# PEER routing: radix-select loops rewritten (SGPR-pair compare masks, straight-line exit test) on top of v1
# speedup vs baseline: 1.0292x; 1.0233x over previous
.LBB0_1813:
	v_lshl_or_b32 v18, 1, s16, v12
	v_cmp_ge_u32_e64 s[58:59], v17, v18
	v_cmp_ge_u32_e64 s[60:61], v19, v18
	v_cmp_ge_u32_e64 s[62:63], v16, v18
	v_cmp_ge_u32_e64 s[64:65], v15, v18
	v_cmp_ge_u32_e64 s[66:67], v14, v18
	v_cmp_ge_u32_e64 s[68:69], v13, v18
	v_cmp_ge_u32_e64 s[70:71], v11, v18
	v_cmp_ge_u32_e64 s[72:73], v10, v18
	v_cndmask_b32_e64 v20, 0, 1, s[58:59]
	v_addc_co_u32_e64 v20, s[74:75], 0, v20, s[60:61]
	v_cndmask_b32_e64 v21, 0, 1, s[62:63]
	v_addc_co_u32_e64 v20, s[74:75], v20, v21, s[64:65]
	v_cndmask_b32_e64 v21, 0, 1, s[66:67]
	v_addc_co_u32_e64 v20, s[74:75], v20, v21, s[68:69]
	v_cndmask_b32_e64 v21, 0, 1, s[70:71]
	v_addc_co_u32_e64 v20, s[74:75], v20, v21, s[72:73]
	s_nop 1
	v_add_u32_dpp v20, v20, v20 row_ror:8 row_mask:0xf bank_mask:0xf bound_ctrl:1
	s_nop 1
	v_add_u32_dpp v20, v20, v20 row_ror:4 row_mask:0xf bank_mask:0xf bound_ctrl:1
	s_nop 1
	v_add_u32_dpp v20, v20, v20 row_ror:2 row_mask:0xf bank_mask:0xf bound_ctrl:1
	s_nop 1
	v_add_u32_dpp v20, v20, v20 row_ror:1 row_mask:0xf bank_mask:0xf bound_ctrl:1
	v_cmp_gt_i32_e64 s[6:7], 16, v20
	v_cmp_eq_u32_e64 s[8:9], 16, v20
	s_nop 0
	s_or_b64 s[6:7], s[10:11], s[6:7]
	s_or_b64 s[10:11], s[10:11], s[8:9]
	v_cndmask_b32_e64 v12, v18, v12, s[6:7]
	s_bitcmp1_b32 s16, 0
	s_cbranch_scc1 .Lsel1_next
	s_cmp_eq_u32 s16, 0
	s_cbranch_scc1 .LBB0_1821
	s_andn2_b64 s[8:9], exec, s[10:11]
	s_cbranch_scc0 .LBB0_1821
.Lsel1_next:
	s_add_i32 s16, s16, -1
	s_branch .LBB0_1813

.LBB0_1855:
	v_lshl_or_b32 v17, 1, s16, v12
	v_cmp_ge_u32_e64 s[58:59], v18, v17
	v_cmp_ge_u32_e64 s[60:61], v19, v17
	v_cmp_ge_u32_e64 s[62:63], v16, v17
	v_cmp_ge_u32_e64 s[64:65], v15, v17
	v_cmp_ge_u32_e64 s[66:67], v14, v17
	v_cmp_ge_u32_e64 s[68:69], v13, v17
	v_cmp_ge_u32_e64 s[70:71], v11, v17
	v_cmp_ge_u32_e64 s[72:73], v10, v17
	v_cndmask_b32_e64 v20, 0, 1, s[58:59]
	v_addc_co_u32_e64 v20, s[74:75], 0, v20, s[60:61]
	v_cndmask_b32_e64 v21, 0, 1, s[62:63]
	v_addc_co_u32_e64 v20, s[74:75], v20, v21, s[64:65]
	v_cndmask_b32_e64 v21, 0, 1, s[66:67]
	v_addc_co_u32_e64 v20, s[74:75], v20, v21, s[68:69]
	v_cndmask_b32_e64 v21, 0, 1, s[70:71]
	v_addc_co_u32_e64 v20, s[74:75], v20, v21, s[72:73]
	s_nop 1
	v_add_u32_dpp v20, v20, v20 row_ror:8 row_mask:0xf bank_mask:0xf bound_ctrl:1
	s_nop 1
	v_add_u32_dpp v20, v20, v20 row_ror:4 row_mask:0xf bank_mask:0xf bound_ctrl:1
	s_nop 1
	v_add_u32_dpp v20, v20, v20 row_ror:2 row_mask:0xf bank_mask:0xf bound_ctrl:1
	s_nop 1
	v_add_u32_dpp v20, v20, v20 row_ror:1 row_mask:0xf bank_mask:0xf bound_ctrl:1
	v_cmp_gt_i32_e64 s[6:7], 16, v20
	v_cmp_eq_u32_e64 s[8:9], 16, v20
	s_nop 0
	s_or_b64 s[6:7], s[10:11], s[6:7]
	s_or_b64 s[10:11], s[10:11], s[8:9]
	v_cndmask_b32_e64 v12, v17, v12, s[6:7]
	s_bitcmp1_b32 s16, 0
	s_cbranch_scc1 .Lsel2_next
	s_cmp_eq_u32 s16, 0
	s_cbranch_scc1 .LBB0_1863
	s_andn2_b64 s[8:9], exec, s[10:11]
	s_cbranch_scc0 .LBB0_1863

.LBB0_1895:
	v_lshl_or_b32 v40, 1, s16, v26
	v_cmp_ge_u32_e64 s[58:59], v32, v40
	v_cmp_ge_u32_e64 s[60:61], v34, v40
	v_cmp_ge_u32_e64 s[62:63], v30, v40
	v_cmp_ge_u32_e64 s[64:65], v28, v40
	v_cmp_ge_u32_e64 s[66:67], v24, v40
	v_cmp_ge_u32_e64 s[68:69], v22, v40
	v_cmp_ge_u32_e64 s[70:71], v20, v40
	v_cmp_ge_u32_e64 s[72:73], v18, v40
	v_cmp_ge_u32_e64 s[74:75], v16, v40
	v_cmp_ge_u32_e64 s[76:77], v14, v40
	v_cmp_ge_u32_e64 s[78:79], v12, v40
	v_cmp_ge_u32_e64 s[80:81], v10, v40
	v_cmp_ge_u32_e64 s[82:83], v8, v40
	v_cmp_ge_u32_e64 s[86:87], v6, v40
	v_cmp_ge_u32_e64 s[88:89], v4, v40
	v_cmp_ge_u32_e64 s[90:91], v2, v40
	v_cndmask_b32_e64 v42, 0, 1, s[58:59]
	v_addc_co_u32_e64 v42, s[92:93], 0, v42, s[60:61]
	v_cndmask_b32_e64 v44, 0, 1, s[62:63]
	v_addc_co_u32_e64 v42, s[92:93], v42, v44, s[64:65]
	v_cndmask_b32_e64 v44, 0, 1, s[66:67]
	v_addc_co_u32_e64 v42, s[92:93], v42, v44, s[68:69]
	v_cndmask_b32_e64 v44, 0, 1, s[70:71]
	v_addc_co_u32_e64 v42, s[92:93], v42, v44, s[72:73]
	v_cndmask_b32_e64 v44, 0, 1, s[74:75]
	v_addc_co_u32_e64 v42, s[92:93], v42, v44, s[76:77]
	v_cndmask_b32_e64 v44, 0, 1, s[78:79]
	v_addc_co_u32_e64 v42, s[92:93], v42, v44, s[80:81]
	v_cndmask_b32_e64 v44, 0, 1, s[82:83]
	v_addc_co_u32_e64 v42, s[92:93], v42, v44, s[86:87]
	v_cndmask_b32_e64 v44, 0, 1, s[88:89]
	v_addc_co_u32_e64 v42, s[92:93], v42, v44, s[90:91]
	s_nop 1
	v_add_u32_dpp v42, v42, v42 row_ror:8 row_mask:0xf bank_mask:0xf bound_ctrl:1
	s_nop 1
	v_add_u32_dpp v42, v42, v42 row_ror:4 row_mask:0xf bank_mask:0xf bound_ctrl:1
	s_nop 1
	v_add_u32_dpp v42, v42, v42 row_ror:2 row_mask:0xf bank_mask:0xf bound_ctrl:1
	s_nop 1
	v_add_u32_dpp v42, v42, v42 row_ror:1 row_mask:0xf bank_mask:0xf bound_ctrl:1
	v_cmp_gt_i32_e64 s[6:7], 16, v42
	v_cmp_eq_u32_e64 s[8:9], 16, v42
	s_nop 0
	s_or_b64 s[6:7], s[10:11], s[6:7]
	s_or_b64 s[10:11], s[10:11], s[8:9]
	v_cndmask_b32_e64 v26, v40, v26, s[6:7]
	s_bitcmp1_b32 s16, 0
	s_cbranch_scc1 .Lsel3_next
	s_cmp_eq_u32 s16, 0
	s_cbranch_scc1 .LBB0_1904
	s_andn2_b64 s[8:9], exec, s[10:11]
	s_cbranch_scc0 .LBB0_1904
